# conversion stores made write-through (sc0 sc1) so the following barrier's L2 write-back has less to flush
# speedup vs baseline: 1.0192x; 1.0075x over previous
.Lcvt_common:
	v_lshlrev_b32_e32 v6, s16, v4
	v_lshl_add_u32 v6, v5, 4, v6
	s_waitcnt lgkmcnt(0)
	s_add_u32 s10, s10, s20
	s_addc_u32 s11, s11, s21
	s_add_i32 s17, s16, 7
	s_lshl_b32 s17, s12, s17
	s_add_u32 s10, s10, s17
	s_addc_u32 s11, s11, 0
	s_lshl_b32 s17, s13, 7
	s_add_u32 s10, s10, s17
	s_addc_u32 s11, s11, 0
	s_add_i32 s17, s16, 3
	s_lshl_b32 s17, 1, s17
	global_load_dwordx4 v[16:19], v6, s[10:11] nt
	s_add_u32 s10, s10, s17
	s_addc_u32 s11, s11, 0
	global_load_dwordx4 v[20:23], v6, s[10:11] nt
	s_add_u32 s10, s10, s17
	s_addc_u32 s11, s11, 0
	global_load_dwordx4 v[24:27], v6, s[10:11] nt
	s_add_u32 s10, s10, s17
	s_addc_u32 s11, s11, 0
	global_load_dwordx4 v[28:31], v6, s[10:11] nt
	s_add_u32 s10, s10, s17
	s_addc_u32 s11, s11, 0
	global_load_dwordx4 v[32:35], v6, s[10:11] nt
	s_add_u32 s10, s10, s17
	s_addc_u32 s11, s11, 0
	global_load_dwordx4 v[36:39], v6, s[10:11] nt
	s_add_u32 s10, s10, s17
	s_addc_u32 s11, s11, 0
	global_load_dwordx4 v[40:43], v6, s[10:11] nt
	s_add_u32 s10, s10, s17
	s_addc_u32 s11, s11, 0
	global_load_dwordx4 v[44:47], v6, s[10:11] nt
	s_add_u32 s10, s10, s17
	s_addc_u32 s11, s11, 0
	global_load_dwordx4 v[48:51], v6, s[10:11] nt
	s_add_u32 s10, s10, s17
	s_addc_u32 s11, s11, 0
	global_load_dwordx4 v[52:55], v6, s[10:11] nt
	s_add_u32 s10, s10, s17
	s_addc_u32 s11, s11, 0
	global_load_dwordx4 v[56:59], v6, s[10:11] nt
	s_add_u32 s10, s10, s17
	s_addc_u32 s11, s11, 0
	global_load_dwordx4 v[60:63], v6, s[10:11] nt
	s_add_u32 s10, s10, s17
	s_addc_u32 s11, s11, 0
	global_load_dwordx4 v[64:67], v6, s[10:11] nt
	s_add_u32 s10, s10, s17
	s_addc_u32 s11, s11, 0
	global_load_dwordx4 v[68:71], v6, s[10:11] nt
	s_add_u32 s10, s10, s17
	s_addc_u32 s11, s11, 0
	global_load_dwordx4 v[72:75], v6, s[10:11] nt
	s_add_u32 s10, s10, s17
	s_addc_u32 s11, s11, 0
	global_load_dwordx4 v[76:79], v6, s[10:11] nt
	s_add_u32 s22, s22, s2
	s_addc_u32 s23, s23, s3
	s_add_u32 s22, s22, s24
	s_addc_u32 s23, s23, 0
	s_lshl_b32 s17, s14, 15
	s_add_u32 s22, s22, s17
	s_addc_u32 s23, s23, 0
	s_lshl_b32 s17, s12, 7
	s_add_u32 s22, s22, s17
	s_addc_u32 s23, s23, 0
	s_mov_b32 s28, 0x0f0f0f0f
	s_mov_b32 s29, 0x0f0f0f0f
	s_mov_b64 exec, s[28:29]
	s_waitcnt vmcnt(15)
	v_mul_f32_e32 v80, 0x42000000, v16
	v_mul_f32_e32 v81, 0x42000000, v17
	v_mul_f32_e32 v82, 0x42000000, v18
	v_mul_f32_e32 v83, 0x42000000, v19
	ds_write_b32 v7, v80 offset:0
	ds_write_b32 v7, v81 offset:4
	ds_write_b32 v7, v82 offset:8
	ds_write_b32 v7, v83 offset:12
	s_waitcnt vmcnt(14)
	v_mul_f32_e32 v80, 0x42000000, v20
	v_mul_f32_e32 v81, 0x42000000, v21
	v_mul_f32_e32 v82, 0x42000000, v22
	v_mul_f32_e32 v83, 0x42000000, v23
	ds_write_b32 v7, v80 offset:544
	ds_write_b32 v7, v81 offset:548
	ds_write_b32 v7, v82 offset:552
	ds_write_b32 v7, v83 offset:556
	s_waitcnt vmcnt(13)
	v_mul_f32_e32 v80, 0x42000000, v24
	v_mul_f32_e32 v81, 0x42000000, v25
	v_mul_f32_e32 v82, 0x42000000, v26
	v_mul_f32_e32 v83, 0x42000000, v27
	ds_write_b32 v7, v80 offset:1088
	ds_write_b32 v7, v81 offset:1092
	ds_write_b32 v7, v82 offset:1096
	ds_write_b32 v7, v83 offset:1100
	s_waitcnt vmcnt(12)
	v_mul_f32_e32 v80, 0x42000000, v28
	v_mul_f32_e32 v81, 0x42000000, v29
	v_mul_f32_e32 v82, 0x42000000, v30
	v_mul_f32_e32 v83, 0x42000000, v31
	ds_write_b32 v7, v80 offset:1632
	ds_write_b32 v7, v81 offset:1636
	ds_write_b32 v7, v82 offset:1640
	ds_write_b32 v7, v83 offset:1644
	s_waitcnt vmcnt(11)
	v_mul_f32_e32 v80, 0x42000000, v32
	v_mul_f32_e32 v81, 0x42000000, v33
	v_mul_f32_e32 v82, 0x42000000, v34
	v_mul_f32_e32 v83, 0x42000000, v35
	ds_write_b32 v7, v80 offset:2176
	ds_write_b32 v7, v81 offset:2180
	ds_write_b32 v7, v82 offset:2184
	ds_write_b32 v7, v83 offset:2188
	s_waitcnt vmcnt(10)
	v_mul_f32_e32 v80, 0x42000000, v36
	v_mul_f32_e32 v81, 0x42000000, v37
	v_mul_f32_e32 v82, 0x42000000, v38
	v_mul_f32_e32 v83, 0x42000000, v39
	ds_write_b32 v7, v80 offset:2720
	ds_write_b32 v7, v81 offset:2724
	ds_write_b32 v7, v82 offset:2728
	ds_write_b32 v7, v83 offset:2732
	s_waitcnt vmcnt(9)
	v_mul_f32_e32 v80, 0x42000000, v40
	v_mul_f32_e32 v81, 0x42000000, v41
	v_mul_f32_e32 v82, 0x42000000, v42
	v_mul_f32_e32 v83, 0x42000000, v43
	ds_write_b32 v7, v80 offset:3264
	ds_write_b32 v7, v81 offset:3268
	ds_write_b32 v7, v82 offset:3272
	ds_write_b32 v7, v83 offset:3276
	s_waitcnt vmcnt(8)
	v_mul_f32_e32 v80, 0x42000000, v44
	v_mul_f32_e32 v81, 0x42000000, v45
	v_mul_f32_e32 v82, 0x42000000, v46
	v_mul_f32_e32 v83, 0x42000000, v47
	ds_write_b32 v7, v80 offset:3808
	ds_write_b32 v7, v81 offset:3812
	ds_write_b32 v7, v82 offset:3816
	ds_write_b32 v7, v83 offset:3820
	s_waitcnt vmcnt(7)
	v_mul_f32_e32 v80, 0x42000000, v48
	v_mul_f32_e32 v81, 0x42000000, v49
	v_mul_f32_e32 v82, 0x42000000, v50
	v_mul_f32_e32 v83, 0x42000000, v51
	ds_write_b32 v7, v80 offset:4352
	ds_write_b32 v7, v81 offset:4356
	ds_write_b32 v7, v82 offset:4360
	ds_write_b32 v7, v83 offset:4364
	s_waitcnt vmcnt(6)
	v_mul_f32_e32 v80, 0x42000000, v52
	v_mul_f32_e32 v81, 0x42000000, v53
	v_mul_f32_e32 v82, 0x42000000, v54
	v_mul_f32_e32 v83, 0x42000000, v55
	ds_write_b32 v7, v80 offset:4896
	ds_write_b32 v7, v81 offset:4900
	ds_write_b32 v7, v82 offset:4904
	ds_write_b32 v7, v83 offset:4908
	s_waitcnt vmcnt(5)
	v_mul_f32_e32 v80, 0x42000000, v56
	v_mul_f32_e32 v81, 0x42000000, v57
	v_mul_f32_e32 v82, 0x42000000, v58
	v_mul_f32_e32 v83, 0x42000000, v59
	ds_write_b32 v7, v80 offset:5440
	ds_write_b32 v7, v81 offset:5444
	ds_write_b32 v7, v82 offset:5448
	ds_write_b32 v7, v83 offset:5452
	s_waitcnt vmcnt(4)
	v_mul_f32_e32 v80, 0x42000000, v60
	v_mul_f32_e32 v81, 0x42000000, v61
	v_mul_f32_e32 v82, 0x42000000, v62
	v_mul_f32_e32 v83, 0x42000000, v63
	ds_write_b32 v7, v80 offset:5984
	ds_write_b32 v7, v81 offset:5988
	ds_write_b32 v7, v82 offset:5992
	ds_write_b32 v7, v83 offset:5996
	s_waitcnt vmcnt(3)
	v_mul_f32_e32 v80, 0x42000000, v64
	v_mul_f32_e32 v81, 0x42000000, v65
	v_mul_f32_e32 v82, 0x42000000, v66
	v_mul_f32_e32 v83, 0x42000000, v67
	ds_write_b32 v7, v80 offset:6528
	ds_write_b32 v7, v81 offset:6532
	ds_write_b32 v7, v82 offset:6536
	ds_write_b32 v7, v83 offset:6540
	s_waitcnt vmcnt(2)
	v_mul_f32_e32 v80, 0x42000000, v68
	v_mul_f32_e32 v81, 0x42000000, v69
	v_mul_f32_e32 v82, 0x42000000, v70
	v_mul_f32_e32 v83, 0x42000000, v71
	ds_write_b32 v7, v80 offset:7072
	ds_write_b32 v7, v81 offset:7076
	ds_write_b32 v7, v82 offset:7080
	ds_write_b32 v7, v83 offset:7084
	s_waitcnt vmcnt(1)
	v_mul_f32_e32 v80, 0x42000000, v72
	v_mul_f32_e32 v81, 0x42000000, v73
	v_mul_f32_e32 v82, 0x42000000, v74
	v_mul_f32_e32 v83, 0x42000000, v75
	ds_write_b32 v7, v80 offset:7616
	ds_write_b32 v7, v81 offset:7620
	ds_write_b32 v7, v82 offset:7624
	ds_write_b32 v7, v83 offset:7628
	s_waitcnt vmcnt(0)
	v_mul_f32_e32 v80, 0x42000000, v76
	v_mul_f32_e32 v81, 0x42000000, v77
	v_mul_f32_e32 v82, 0x42000000, v78
	v_mul_f32_e32 v83, 0x42000000, v79
	ds_write_b32 v7, v80 offset:8160
	ds_write_b32 v7, v81 offset:8164
	ds_write_b32 v7, v82 offset:8168
	ds_write_b32 v7, v83 offset:8172
	s_mov_b64 exec, -1
	s_waitcnt lgkmcnt(0)
	ds_read_b32 v84, v8 offset:0
	ds_read_b32 v85, v8 offset:68
	ds_read_b32 v86, v8 offset:136
	ds_read_b32 v87, v8 offset:204
	ds_read_b32 v88, v8 offset:272
	ds_read_b32 v89, v8 offset:340
	ds_read_b32 v90, v8 offset:408
	ds_read_b32 v91, v8 offset:476
	ds_read_b32 v92, v8 offset:544
	ds_read_b32 v93, v8 offset:612
	ds_read_b32 v94, v8 offset:680
	ds_read_b32 v95, v8 offset:748
	ds_read_b32 v96, v8 offset:816
	ds_read_b32 v97, v8 offset:884
	ds_read_b32 v98, v8 offset:952
	ds_read_b32 v99, v8 offset:1020
	s_waitcnt lgkmcnt(0)
	v_cvt_pk_fp8_f32 v100, v84, v85
	s_nop 0
	v_cvt_pk_fp8_f32 v100, v86, v87 op_sel:[0,0,1]
	v_cvt_pk_fp8_f32 v101, v88, v89
	s_nop 0
	v_cvt_pk_fp8_f32 v101, v90, v91 op_sel:[0,0,1]
	v_cvt_pk_fp8_f32 v102, v92, v93
	s_nop 0
	v_cvt_pk_fp8_f32 v102, v94, v95 op_sel:[0,0,1]
	v_cvt_pk_fp8_f32 v103, v96, v97
	s_nop 0
	v_cvt_pk_fp8_f32 v103, v98, v99 op_sel:[0,0,1]
	s_nop 0
	global_store_dwordx4 v9, v[100:103], s[22:23] sc0 sc1
	s_nop 1
	ds_read_b32 v84, v8 offset:32
	ds_read_b32 v85, v8 offset:100
	ds_read_b32 v86, v8 offset:168
	ds_read_b32 v87, v8 offset:236
	ds_read_b32 v88, v8 offset:304
	ds_read_b32 v89, v8 offset:372
	ds_read_b32 v90, v8 offset:440
	ds_read_b32 v91, v8 offset:508
	ds_read_b32 v92, v8 offset:576
	ds_read_b32 v93, v8 offset:644
	ds_read_b32 v94, v8 offset:712
	ds_read_b32 v95, v8 offset:780
	ds_read_b32 v96, v8 offset:848
	ds_read_b32 v97, v8 offset:916
	ds_read_b32 v98, v8 offset:984
	ds_read_b32 v99, v8 offset:1052
	s_waitcnt lgkmcnt(0)
	v_cvt_pk_fp8_f32 v100, v84, v85
	s_nop 0
	v_cvt_pk_fp8_f32 v100, v86, v87 op_sel:[0,0,1]
	v_cvt_pk_fp8_f32 v101, v88, v89
	s_nop 0
	v_cvt_pk_fp8_f32 v101, v90, v91 op_sel:[0,0,1]
	v_cvt_pk_fp8_f32 v102, v92, v93
	s_nop 0
	v_cvt_pk_fp8_f32 v102, v94, v95 op_sel:[0,0,1]
	v_cvt_pk_fp8_f32 v103, v96, v97
	s_nop 0
	v_cvt_pk_fp8_f32 v103, v98, v99 op_sel:[0,0,1]
	s_nop 0
	global_store_dwordx4 v10, v[100:103], s[22:23] sc0 sc1
	s_nop 1
	s_waitcnt lgkmcnt(0)
	s_not_b64 s[28:29], s[28:29]
	s_add_u32 s22, s22, 0x4000
	s_addc_u32 s23, s23, 0
	s_mov_b64 exec, s[28:29]
	v_mul_f32_e32 v80, 0x42000000, v16
	v_mul_f32_e32 v81, 0x42000000, v17
	v_mul_f32_e32 v82, 0x42000000, v18
	v_mul_f32_e32 v83, 0x42000000, v19
	ds_write_b32 v7, v80 offset:0
	ds_write_b32 v7, v81 offset:4
	ds_write_b32 v7, v82 offset:8
	ds_write_b32 v7, v83 offset:12
	v_mul_f32_e32 v80, 0x42000000, v20
	v_mul_f32_e32 v81, 0x42000000, v21
	v_mul_f32_e32 v82, 0x42000000, v22
	v_mul_f32_e32 v83, 0x42000000, v23
	ds_write_b32 v7, v80 offset:544
	ds_write_b32 v7, v81 offset:548
	ds_write_b32 v7, v82 offset:552
	ds_write_b32 v7, v83 offset:556
	v_mul_f32_e32 v80, 0x42000000, v24
	v_mul_f32_e32 v81, 0x42000000, v25
	v_mul_f32_e32 v82, 0x42000000, v26
	v_mul_f32_e32 v83, 0x42000000, v27
	ds_write_b32 v7, v80 offset:1088
	ds_write_b32 v7, v81 offset:1092
	ds_write_b32 v7, v82 offset:1096
	ds_write_b32 v7, v83 offset:1100
	v_mul_f32_e32 v80, 0x42000000, v28
	v_mul_f32_e32 v81, 0x42000000, v29
	v_mul_f32_e32 v82, 0x42000000, v30
	v_mul_f32_e32 v83, 0x42000000, v31
	ds_write_b32 v7, v80 offset:1632
	ds_write_b32 v7, v81 offset:1636
	ds_write_b32 v7, v82 offset:1640
	ds_write_b32 v7, v83 offset:1644
	v_mul_f32_e32 v80, 0x42000000, v32
	v_mul_f32_e32 v81, 0x42000000, v33
	v_mul_f32_e32 v82, 0x42000000, v34
	v_mul_f32_e32 v83, 0x42000000, v35
	ds_write_b32 v7, v80 offset:2176
	ds_write_b32 v7, v81 offset:2180
	ds_write_b32 v7, v82 offset:2184
	ds_write_b32 v7, v83 offset:2188
	v_mul_f32_e32 v80, 0x42000000, v36
	v_mul_f32_e32 v81, 0x42000000, v37
	v_mul_f32_e32 v82, 0x42000000, v38
	v_mul_f32_e32 v83, 0x42000000, v39
	ds_write_b32 v7, v80 offset:2720
	ds_write_b32 v7, v81 offset:2724
	ds_write_b32 v7, v82 offset:2728
	ds_write_b32 v7, v83 offset:2732
	v_mul_f32_e32 v80, 0x42000000, v40
	v_mul_f32_e32 v81, 0x42000000, v41
	v_mul_f32_e32 v82, 0x42000000, v42
	v_mul_f32_e32 v83, 0x42000000, v43
	ds_write_b32 v7, v80 offset:3264
	ds_write_b32 v7, v81 offset:3268
	ds_write_b32 v7, v82 offset:3272
	ds_write_b32 v7, v83 offset:3276
	v_mul_f32_e32 v80, 0x42000000, v44
	v_mul_f32_e32 v81, 0x42000000, v45
	v_mul_f32_e32 v82, 0x42000000, v46
	v_mul_f32_e32 v83, 0x42000000, v47
	ds_write_b32 v7, v80 offset:3808
	ds_write_b32 v7, v81 offset:3812
	ds_write_b32 v7, v82 offset:3816
	ds_write_b32 v7, v83 offset:3820
	v_mul_f32_e32 v80, 0x42000000, v48
	v_mul_f32_e32 v81, 0x42000000, v49
	v_mul_f32_e32 v82, 0x42000000, v50
	v_mul_f32_e32 v83, 0x42000000, v51
	ds_write_b32 v7, v80 offset:4352
	ds_write_b32 v7, v81 offset:4356
	ds_write_b32 v7, v82 offset:4360
	ds_write_b32 v7, v83 offset:4364
	v_mul_f32_e32 v80, 0x42000000, v52
	v_mul_f32_e32 v81, 0x42000000, v53
	v_mul_f32_e32 v82, 0x42000000, v54
	v_mul_f32_e32 v83, 0x42000000, v55
	ds_write_b32 v7, v80 offset:4896
	ds_write_b32 v7, v81 offset:4900
	ds_write_b32 v7, v82 offset:4904
	ds_write_b32 v7, v83 offset:4908
	v_mul_f32_e32 v80, 0x42000000, v56
	v_mul_f32_e32 v81, 0x42000000, v57
	v_mul_f32_e32 v82, 0x42000000, v58
	v_mul_f32_e32 v83, 0x42000000, v59
	ds_write_b32 v7, v80 offset:5440
	ds_write_b32 v7, v81 offset:5444
	ds_write_b32 v7, v82 offset:5448
	ds_write_b32 v7, v83 offset:5452
	v_mul_f32_e32 v80, 0x42000000, v60
	v_mul_f32_e32 v81, 0x42000000, v61
	v_mul_f32_e32 v82, 0x42000000, v62
	v_mul_f32_e32 v83, 0x42000000, v63
	ds_write_b32 v7, v80 offset:5984
	ds_write_b32 v7, v81 offset:5988
	ds_write_b32 v7, v82 offset:5992
	ds_write_b32 v7, v83 offset:5996
	v_mul_f32_e32 v80, 0x42000000, v64
	v_mul_f32_e32 v81, 0x42000000, v65
	v_mul_f32_e32 v82, 0x42000000, v66
	v_mul_f32_e32 v83, 0x42000000, v67
	ds_write_b32 v7, v80 offset:6528
	ds_write_b32 v7, v81 offset:6532
	ds_write_b32 v7, v82 offset:6536
	ds_write_b32 v7, v83 offset:6540
	v_mul_f32_e32 v80, 0x42000000, v68
	v_mul_f32_e32 v81, 0x42000000, v69
	v_mul_f32_e32 v82, 0x42000000, v70
	v_mul_f32_e32 v83, 0x42000000, v71
	ds_write_b32 v7, v80 offset:7072
	ds_write_b32 v7, v81 offset:7076
	ds_write_b32 v7, v82 offset:7080
	ds_write_b32 v7, v83 offset:7084
	v_mul_f32_e32 v80, 0x42000000, v72
	v_mul_f32_e32 v81, 0x42000000, v73
	v_mul_f32_e32 v82, 0x42000000, v74
	v_mul_f32_e32 v83, 0x42000000, v75
	ds_write_b32 v7, v80 offset:7616
	ds_write_b32 v7, v81 offset:7620
	ds_write_b32 v7, v82 offset:7624
	ds_write_b32 v7, v83 offset:7628
	v_mul_f32_e32 v80, 0x42000000, v76
	v_mul_f32_e32 v81, 0x42000000, v77
	v_mul_f32_e32 v82, 0x42000000, v78
	v_mul_f32_e32 v83, 0x42000000, v79
	ds_write_b32 v7, v80 offset:8160
	ds_write_b32 v7, v81 offset:8164
	ds_write_b32 v7, v82 offset:8168
	ds_write_b32 v7, v83 offset:8172
	s_mov_b64 exec, -1
	s_waitcnt lgkmcnt(0)
	ds_read_b32 v84, v8 offset:0
	ds_read_b32 v85, v8 offset:68
	ds_read_b32 v86, v8 offset:136
	ds_read_b32 v87, v8 offset:204
	ds_read_b32 v88, v8 offset:272
	ds_read_b32 v89, v8 offset:340
	ds_read_b32 v90, v8 offset:408
	ds_read_b32 v91, v8 offset:476
	ds_read_b32 v92, v8 offset:544
	ds_read_b32 v93, v8 offset:612
	ds_read_b32 v94, v8 offset:680
	ds_read_b32 v95, v8 offset:748
	ds_read_b32 v96, v8 offset:816
	ds_read_b32 v97, v8 offset:884
	ds_read_b32 v98, v8 offset:952
	ds_read_b32 v99, v8 offset:1020
	s_waitcnt lgkmcnt(0)
	v_cvt_pk_fp8_f32 v100, v84, v85
	s_nop 0
	v_cvt_pk_fp8_f32 v100, v86, v87 op_sel:[0,0,1]
	v_cvt_pk_fp8_f32 v101, v88, v89
	s_nop 0
	v_cvt_pk_fp8_f32 v101, v90, v91 op_sel:[0,0,1]
	v_cvt_pk_fp8_f32 v102, v92, v93
	s_nop 0
	v_cvt_pk_fp8_f32 v102, v94, v95 op_sel:[0,0,1]
	v_cvt_pk_fp8_f32 v103, v96, v97
	s_nop 0
	v_cvt_pk_fp8_f32 v103, v98, v99 op_sel:[0,0,1]
	s_nop 0
	global_store_dwordx4 v9, v[100:103], s[22:23] sc0 sc1
	s_nop 1
	ds_read_b32 v84, v8 offset:32
	ds_read_b32 v85, v8 offset:100
	ds_read_b32 v86, v8 offset:168
	ds_read_b32 v87, v8 offset:236
	ds_read_b32 v88, v8 offset:304
	ds_read_b32 v89, v8 offset:372
	ds_read_b32 v90, v8 offset:440
	ds_read_b32 v91, v8 offset:508
	ds_read_b32 v92, v8 offset:576
	ds_read_b32 v93, v8 offset:644
	ds_read_b32 v94, v8 offset:712
	ds_read_b32 v95, v8 offset:780
	ds_read_b32 v96, v8 offset:848
	ds_read_b32 v97, v8 offset:916
	ds_read_b32 v98, v8 offset:984
	ds_read_b32 v99, v8 offset:1052
	s_waitcnt lgkmcnt(0)
	v_cvt_pk_fp8_f32 v100, v84, v85
	s_nop 0
	v_cvt_pk_fp8_f32 v100, v86, v87 op_sel:[0,0,1]
	v_cvt_pk_fp8_f32 v101, v88, v89
	s_nop 0
	v_cvt_pk_fp8_f32 v101, v90, v91 op_sel:[0,0,1]
	v_cvt_pk_fp8_f32 v102, v92, v93
	s_nop 0
	v_cvt_pk_fp8_f32 v102, v94, v95 op_sel:[0,0,1]
	v_cvt_pk_fp8_f32 v103, v96, v97
	s_nop 0
	v_cvt_pk_fp8_f32 v103, v98, v99 op_sel:[0,0,1]
	s_nop 0
	global_store_dwordx4 v10, v[100:103], s[22:23] sc0 sc1
	s_nop 1
	s_add_i32 s30, s30, s25
	s_add_i32 s26, s26, -1
	s_cmp_lg_u32 s26, 0
	s_cbranch_scc1 .Lcvt_item
